# static priority raise (s_setprio 1) for the waves of the second attention unit of each workgroup through the unit loop, reset at role exit
# speedup vs baseline: 1.0056x; 1.0017x over previous
.LBB0_420:
	s_ashr_i32 s2, s1, 6
	s_add_u32 s84, s6, 0x8000000
	s_addc_u32 s85, s7, 0
	s_ashr_i32 s4, s1, 8
	s_cmp_eq_u32 s4, 0
	s_cbranch_scc1 .Latt_prio0
	s_setprio 1
.Latt_prio0:
	s_lshl_b32 s21, s2, 5
	s_lshl_b32 s1, s2, 14
	s_and_b32 s3, s21, 0x60
	s_lshl_b32 s75, s4, 16
	s_lshl_b32 s1, s3, 7
	s_add_i32 s75, s75, s1
	v_and_b32_e32 v8, 63, v4
	s_cmp_gt_i32 s0, 0
	v_and_b32_e32 v7, 31, v4
	v_bfe_u32 v6, v4, 5, 1
	s_mov_b32 s86, 0
	s_mov_b32 s81, 1
	s_cselect_b64 s[8:9], -1, 0
	s_cmp_lt_i32 s0, 1
	v_lshrrev_b32_e32 v5, 3, v8
	v_writelane_b32 v254, s4, 14
	s_cbranch_scc1 .LBB0_428
	s_lshl_b32 s1, s90, 1
	s_add_i32 s1, s4, s1
	s_ashr_i32 s86, s1, 11
	s_bfe_u32 s2, s1, 0x70004
	s_and_b32 s88, s1, 15
	s_lshl_b32 s1, s86, 1
	s_lshr_b32 s33, s2, s1
	s_bfm_b32 s4, s1, 0
	s_and_b32 s2, s4, s2
	s_lshl_b32 s4, s33, 7
	s_or_b32 s12, s21, 0xffffff80
	s_lshl_b32 s4, s4, s1
	v_or_b32_e32 v1, s12, v5
	s_or_b32 s42, s4, s2
	v_lshlrev_b32_e32 v1, s1, v1
	v_add_u32_e32 v1, s42, v1
	s_movk_i32 s2, 0xc40
	v_mul_lo_u32 v1, v1, s2
	s_lshl_b32 s2, s88, 6
	v_bitop3_b32 v2, v5, v4, 7 bitop3:0x78
	v_add_lshl_u32 v1, v1, s2, 1
	v_lshl_or_b32 v2, v2, 4, v1
	s_cmp_lg_u32 s33, 0
	s_cselect_b64 s[10:11], -1, 0
	s_cmp_eq_u32 s33, 0
	v_add_u32_e32 v178, 0x800, v2
	s_cbranch_scc1 .LBB0_504
	v_mov_b32_e32 v179, 0
	v_lshl_add_u64 v[2:3], s[84:85], 0, v[178:179]
	s_lshl_b32 s4, 8, s1
	v_mov_b32_e32 v9, 0x1880
	s_add_i32 m0, s75, 0x2000
	v_mad_i64_i32 v[10:11], s[4:5], s4, v9, v[2:3]
	s_add_i32 m0, s75, 0x2400
	s_lshl_b32 s4, 16, s1
	v_mad_u64_u32 v[10:11], s[4:5], s4, v9, v[2:3]
	s_add_i32 m0, s75, 0x2800
	s_lshl_b32 s4, 24, s1
	v_mad_i64_i32 v[2:3], s[4:5], s4, v9, v[2:3]
	s_cbranch_execnz .LBB0_424

.LBB0_492:
	s_setprio 0
	v_readlane_b32 s0, v254, 1
	s_cmp_gt_i32 s0, 4
	v_readlane_b32 s2, v254, 12
	s_cselect_b64 s[0:1], -1, 0
	v_readlane_b32 s3, v254, 13
	s_and_b64 s[0:1], s[2:3], s[0:1]
	s_andn2_b64 vcc, exec, s[0:1]
	s_cbranch_vccnz .LBB0_539
	s_waitcnt vmcnt(0)
	s_waitcnt vmcnt(0) lgkmcnt(0)
	s_barrier
	s_mov_b64 s[6:7], exec
	v_readlane_b32 s0, v254, 4
	v_readlane_b32 s1, v254, 5
	s_and_b64 s[0:1], s[6:7], s[0:1]
	s_mov_b64 exec, s[0:1]
	s_cbranch_execz .LBB0_538
	v_readlane_b32 s0, v254, 6
	s_waitcnt vmcnt(0) expcnt(0) lgkmcnt(0)
	s_nop 0
	v_mov_b32_e32 v1, s0
	ds_read_b32 v3, v1
	ds_read_b32 v1, v1 offset:4
	s_waitcnt lgkmcnt(1)
	v_cmp_ne_u32_e32 vcc, 0, v3
	s_cbranch_vccnz .LBB0_509
	v_readlane_b32 s2, v254, 2
	v_readlane_b32 s3, v254, 3
	s_add_u32 s8, s76, 0x1000
	s_load_dwordx2 s[0:1], s[2:3], 0x4
	s_addc_u32 s9, s77, 0
	s_add_u32 s10, s76, 0x1100
	s_addc_u32 s11, s77, 0
	s_add_u32 s12, s76, 0x1200
	s_addc_u32 s13, s77, 0
	s_waitcnt lgkmcnt(0)
	s_mul_i32 s0, s0, s74
	s_add_u32 s14, s76, 0x1300
	s_mul_i32 s0, s0, s1
	s_addc_u32 s15, s77, 0
	s_mov_b32 s1, 1
	v_mov_b32_e32 v17, 0
	s_branch .LBB0_497
